# k_node kernels get the XCD-aware (16-workgroup runs) tile assignment too
# speedup vs baseline: 1.0069x; 1.0064x over previous
.LBB7_3:
	v_lshrrev_b32_e32 v1, 6, v0
	s_and_b32 s90, s2, 7
	s_lshl_b32 s90, s90, 4
	s_bfe_u32 s91, s2, 0x40003
	s_or_b32 s90, s90, s91
	s_and_b32 s91, s2, 0xffffff80
	s_or_b32 s90, s90, s91
	s_cmp_lt_u32 s2, 0x180
	s_cselect_b32 s2, s90, s2
	v_lshl_or_b32 v106, s2, 2, v1
	v_and_b32_e32 v107, 31, v0
	v_lshlrev_b32_e32 v114, 5, v106
	v_or_b32_e32 v2, v114, v107
	v_min_i32_e32 v58, 0xc34f, v2
	v_ashrrev_i32_e32 v59, 31, v58
	v_lshl_add_u64 v[2:3], v[58:59], 2, s[4:5]
	global_load_dwordx2 v[108:109], v[2:3], off
	v_lshl_add_u64 v[154:155], v[58:59], 2, s[24:25]
	global_load_dword v154, v[154:155], off
	v_min_i32_e32 v2, 0x61a, v106
	v_lshlrev_b32_e32 v3, 5, v2
	v_sub_u32_e32 v3, 0xc350, v3
	v_min_u32_e32 v3, 32, v3
	v_add_u32_e32 v8, -1, v3
	v_ashrrev_i32_e32 v3, 31, v2
	v_lshlrev_b32_e32 v4, 2, v0
	v_and_b32_e32 v143, 60, v4
	v_bfe_u32 v142, v0, 4, 2
	v_lshlrev_b64 v[2:3], 13, v[2:3]
	v_lshl_add_u64 v[2:3], s[12:13], 0, v[2:3]
	v_lshlrev_b32_e32 v110, 2, v143
	v_or_b32_e32 v140, 4, v142
	v_lshl_add_u64 v[2:3], v[2:3], 0, v[110:111]
	v_lshlrev_b32_e32 v4, 8, v142
	v_mov_b32_e32 v5, v111
	v_lshlrev_b32_e32 v6, 8, v140
	v_mov_b32_e32 v7, v111
	v_lshl_add_u64 v[4:5], v[2:3], 0, v[4:5]
	v_lshl_add_u64 v[6:7], v[2:3], 0, v[6:7]
	v_or_b32_e32 v139, 8, v142
	v_or_b32_e32 v138, 12, v142
	global_load_dwordx4 v[34:37], v[4:5], off
	global_load_dwordx4 v[38:41], v[6:7], off
	v_lshlrev_b32_e32 v4, 8, v139
	v_mov_b32_e32 v5, v111
	v_lshlrev_b32_e32 v6, 8, v138
	v_mov_b32_e32 v7, v111
	v_lshl_add_u64 v[4:5], v[2:3], 0, v[4:5]
	v_lshl_add_u64 v[6:7], v[2:3], 0, v[6:7]
	v_or_b32_e32 v137, 16, v142
	v_or_b32_e32 v136, 20, v142
	global_load_dwordx4 v[42:45], v[4:5], off
	global_load_dwordx4 v[46:49], v[6:7], off
	v_min_u32_e32 v4, v137, v8
	v_min_u32_e32 v6, v136, v8
	v_lshlrev_b32_e32 v4, 8, v4
	v_mov_b32_e32 v5, v111
	v_lshlrev_b32_e32 v6, 8, v6
	v_mov_b32_e32 v7, v111
	v_lshl_add_u64 v[4:5], v[2:3], 0, v[4:5]
	v_lshl_add_u64 v[6:7], v[2:3], 0, v[6:7]
	v_or_b32_e32 v135, 24, v142
	v_or_b32_e32 v134, 28, v142
	global_load_dwordx4 v[82:85], v[4:5], off
	global_load_dwordx4 v[86:89], v[6:7], off
	v_min_u32_e32 v4, v135, v8
	v_min_u32_e32 v6, v134, v8
	v_bfe_u32 v113, v0, 5, 1
	v_lshlrev_b32_e32 v4, 8, v4
	v_mov_b32_e32 v5, v111
	v_lshlrev_b32_e32 v6, 8, v6
	v_mov_b32_e32 v7, v111
	v_lshl_add_u64 v[4:5], v[2:3], 0, v[4:5]
	v_lshl_add_u64 v[2:3], v[2:3], 0, v[6:7]
	v_lshlrev_b32_e32 v144, 4, v113
	global_load_dwordx4 v[90:93], v[4:5], off
	global_load_dwordx4 v[94:97], v[2:3], off
	global_load_dwordx4 v[18:21], v144, s[10:11]
	global_load_dwordx4 v[22:25], v144, s[10:11] offset:32
	global_load_dwordx4 v[26:29], v144, s[10:11] offset:64
	global_load_dwordx4 v[30:33], v144, s[10:11] offset:96
	s_nop 0
	global_load_dwordx4 v[2:5], v144, s[10:11] offset:128
	global_load_dwordx4 v[6:9], v144, s[10:11] offset:160
	global_load_dwordx4 v[10:13], v144, s[10:11] offset:192
	global_load_dwordx4 v[14:17], v144, s[10:11] offset:224
	s_load_dwordx2 s[20:21], s[0:1], 0x10
	s_waitcnt vmcnt(18)
	ds_write_b128 v112, v[54:57] offset:34816
	v_cndmask_b32_e64 v54, 0, 1, s[8:9]
	v_cmp_ne_u32_e64 s[18:19], 1, v54
	s_andn2_b64 vcc, exec, s[8:9]
	s_waitcnt vmcnt(17)
	ds_write_b128 v112, v[50:53] offset:38912
	s_cbranch_vccnz .LBB7_5
	s_load_dwordx4 s[8:11], s[0:1], 0x18
	v_add_u32_e32 v111, 0x8800, v112
	s_waitcnt lgkmcnt(0)
	s_nop 0
	s_nop 0
	v_lshlrev_b32_e32 v50, 2, v113
	v_mov_b32_e32 v51, 0
	v_lshlrev_b32_e32 v50, 2, v50
	s_waitcnt vmcnt(16)
	v_lshlrev_b32_e32 v52, 6, v154
	v_ashrrev_i32_e32 v53, 31, v52
	v_lshl_add_u64 v[52:53], v[52:53], 2, s[10:11]
	v_lshl_add_u64 v[116:117], v[52:53], 0, v[50:51]
	global_load_dwordx4 v[74:77], v[116:117], off
	global_load_dwordx4 v[78:81], v[116:117], off offset:32
	global_load_dwordx4 v[70:73], v[116:117], off offset:64
	global_load_dwordx4 v[66:69], v[116:117], off offset:96
	global_load_dwordx4 v[62:65], v[116:117], off offset:128
	global_load_dwordx4 v[58:61], v[116:117], off offset:160
	global_load_dwordx4 v[54:57], v[116:117], off offset:192
	global_load_dwordx4 v[50:53], v[116:117], off offset:224
	ds_write_b128 v111, v[102:105] offset:16384
	ds_write_b128 v111, v[98:101] offset:20480
	s_branch .LBB7_6

.LBB8_3:
	v_lshrrev_b32_e32 v1, 6, v0
	s_and_b32 s90, s2, 7
	s_lshl_b32 s90, s90, 4
	s_bfe_u32 s91, s2, 0x40003
	s_or_b32 s90, s90, s91
	s_and_b32 s91, s2, 0xffffff80
	s_or_b32 s90, s90, s91
	s_cmp_lt_u32 s2, 0x180
	s_cselect_b32 s2, s90, s2
	v_lshl_or_b32 v172, s2, 2, v1
	v_and_b32_e32 v177, 31, v0
	v_lshlrev_b32_e32 v179, 5, v172
	v_or_b32_e32 v2, v179, v177
	v_min_i32_e32 v62, 0xc34f, v2
	v_ashrrev_i32_e32 v63, 31, v62
	v_lshl_add_u64 v[4:5], v[62:63], 2, s[4:5]
	global_load_dwordx2 v[174:175], v[4:5], off
	v_lshl_add_u64 v[218:219], v[62:63], 2, s[24:25]
	global_load_dword v218, v[218:219], off
	v_min_i32_e32 v4, 0x61a, v172
	v_lshlrev_b32_e32 v2, 5, v4
	v_sub_u32_e32 v2, 0xc350, v2
	v_min_u32_e32 v2, 32, v2
	v_add_u32_e32 v22, -1, v2
	v_ashrrev_i32_e32 v5, 31, v4
	v_lshlrev_b32_e32 v2, 2, v0
	v_and_b32_e32 v207, 60, v2
	v_lshlrev_b64 v[4:5], 13, v[4:5]
	v_bfe_u32 v206, v0, 4, 2
	v_lshl_or_b32 v4, v207, 2, v4
	s_waitcnt lgkmcnt(0)
	v_lshl_add_u64 v[6:7], s[12:13], 0, v[4:5]
	v_lshlrev_b32_e32 v2, 8, v206
	v_or_b32_e32 v204, 4, v206
	v_lshl_add_u64 v[8:9], v[6:7], 0, v[2:3]
	v_lshlrev_b32_e32 v10, 8, v204
	v_mov_b32_e32 v11, v3
	v_or_b32_e32 v203, 8, v206
	v_lshl_add_u64 v[12:13], v[6:7], 0, v[10:11]
	global_load_dwordx4 v[132:135], v[8:9], off
	global_load_dwordx4 v[136:139], v[12:13], off
	v_lshlrev_b32_e32 v8, 8, v203
	v_mov_b32_e32 v9, v3
	v_or_b32_e32 v202, 12, v206
	v_lshl_add_u64 v[12:13], v[6:7], 0, v[8:9]
	v_lshlrev_b32_e32 v14, 8, v202
	v_mov_b32_e32 v15, v3
	v_or_b32_e32 v201, 16, v206
	v_lshl_add_u64 v[16:17], v[6:7], 0, v[14:15]
	global_load_dwordx4 v[140:143], v[12:13], off
	global_load_dwordx4 v[144:147], v[16:17], off
	v_min_u32_e32 v12, v201, v22
	v_or_b32_e32 v200, 20, v206
	v_lshlrev_b32_e32 v12, 8, v12
	v_mov_b32_e32 v13, v3
	v_min_u32_e32 v18, v200, v22
	v_lshl_add_u64 v[16:17], v[6:7], 0, v[12:13]
	v_lshlrev_b32_e32 v18, 8, v18
	v_mov_b32_e32 v19, v3
	v_or_b32_e32 v199, 24, v206
	v_or_b32_e32 v198, 28, v206
	v_lshl_add_u64 v[20:21], v[6:7], 0, v[18:19]
	global_load_dwordx4 v[148:151], v[16:17], off
	global_load_dwordx4 v[152:155], v[20:21], off
	v_min_u32_e32 v16, v199, v22
	v_min_u32_e32 v22, v198, v22
	v_lshlrev_b32_e32 v16, 8, v16
	v_mov_b32_e32 v17, v3
	v_lshlrev_b32_e32 v22, 8, v22
	v_mov_b32_e32 v23, v3
	v_lshl_add_u64 v[4:5], s[14:15], 0, v[4:5]
	v_lshl_add_u64 v[20:21], v[6:7], 0, v[16:17]
	v_lshl_add_u64 v[6:7], v[6:7], 0, v[22:23]
	v_lshl_add_u64 v[2:3], v[4:5], 0, v[2:3]
	global_load_dwordx4 v[156:159], v[20:21], off
	global_load_dwordx4 v[160:163], v[6:7], off
	v_lshl_add_u64 v[6:7], v[4:5], 0, v[10:11]
	global_load_dwordx4 v[104:107], v[2:3], off
	global_load_dwordx4 v[100:103], v[6:7], off
	v_lshl_add_u64 v[2:3], v[4:5], 0, v[8:9]
	v_bfe_u32 v178, v0, 5, 1
	v_lshl_add_u64 v[6:7], v[4:5], 0, v[14:15]
	global_load_dwordx4 v[108:111], v[2:3], off
	global_load_dwordx4 v[112:115], v[6:7], off
	v_lshl_add_u64 v[2:3], v[4:5], 0, v[12:13]
	v_lshl_add_u64 v[6:7], v[4:5], 0, v[18:19]
	global_load_dwordx4 v[116:119], v[2:3], off
	global_load_dwordx4 v[120:123], v[6:7], off
	v_lshl_add_u64 v[2:3], v[4:5], 0, v[16:17]
	v_lshl_add_u64 v[4:5], v[4:5], 0, v[22:23]
	v_lshlrev_b32_e32 v173, 4, v178
	global_load_dwordx4 v[128:131], v[2:3], off
	global_load_dwordx4 v[124:127], v[4:5], off
	global_load_dwordx4 v[18:21], v173, s[10:11]
	global_load_dwordx4 v[22:25], v173, s[10:11] offset:32
	global_load_dwordx4 v[26:29], v173, s[10:11] offset:64
	global_load_dwordx4 v[30:33], v173, s[10:11] offset:96
	s_nop 0
	global_load_dwordx4 v[2:5], v173, s[10:11] offset:128
	global_load_dwordx4 v[6:9], v173, s[10:11] offset:160
	global_load_dwordx4 v[10:13], v173, s[10:11] offset:192
	global_load_dwordx4 v[14:17], v173, s[10:11] offset:224
	global_load_dwordx4 v[96:99], v173, s[18:19]
	global_load_dwordx4 v[92:95], v173, s[18:19] offset:32
	global_load_dwordx4 v[88:91], v173, s[18:19] offset:64
	global_load_dwordx4 v[84:87], v173, s[18:19] offset:96
	global_load_dwordx4 v[80:83], v173, s[18:19] offset:128
	global_load_dwordx4 v[42:45], v173, s[18:19] offset:160
	global_load_dwordx4 v[38:41], v173, s[18:19] offset:192
	global_load_dwordx4 v[34:37], v173, s[18:19] offset:224
	s_load_dwordx2 s[20:21], s[0:1], 0x10
	s_waitcnt vmcnt(36)
	ds_write_b128 v176, v[46:49] offset:34816
	s_waitcnt vmcnt(35)
	ds_write_b128 v176, v[50:53] offset:38912
	s_waitcnt vmcnt(34)
	ds_write_b128 v176, v[58:61] offset:43008
	v_cndmask_b32_e64 v46, 0, 1, s[8:9]
	v_cmp_ne_u32_e64 s[18:19], 1, v46
	s_andn2_b64 vcc, exec, s[8:9]
	s_waitcnt vmcnt(33)
	ds_write_b128 v176, v[54:57] offset:47104
	s_cbranch_vccnz .LBB8_5
	s_load_dwordx4 s[8:11], s[0:1], 0x18
	s_waitcnt lgkmcnt(0)
	s_nop 0
	s_nop 0
	v_lshlrev_b32_e32 v46, 2, v178
	v_mov_b32_e32 v47, 0
	v_lshlrev_b32_e32 v46, 2, v46
	s_waitcnt vmcnt(32)
	v_lshlrev_b32_e32 v48, 6, v218
	v_ashrrev_i32_e32 v49, 31, v48
	v_lshl_add_u64 v[48:49], v[48:49], 2, s[10:11]
	v_lshl_add_u64 v[46:47], v[48:49], 0, v[46:47]
	global_load_dwordx4 v[72:75], v[46:47], off
	global_load_dwordx4 v[76:79], v[46:47], off offset:32
	global_load_dwordx4 v[68:71], v[46:47], off offset:64
	global_load_dwordx4 v[64:67], v[46:47], off offset:96
	global_load_dwordx4 v[60:63], v[46:47], off offset:128
	global_load_dwordx4 v[56:59], v[46:47], off offset:160
	global_load_dwordx4 v[52:55], v[46:47], off offset:192
	global_load_dwordx4 v[48:51], v[46:47], off offset:224
	v_add_u32_e32 v46, 0x8800, v176
	ds_write_b128 v46, v[168:171] offset:16384
	ds_write_b128 v46, v[164:167] offset:20480
	s_branch .LBB8_6

.LBB9_3:
	v_lshrrev_b32_e32 v1, 6, v0
	s_and_b32 s90, s2, 7
	s_lshl_b32 s90, s90, 4
	s_bfe_u32 s91, s2, 0x40003
	s_or_b32 s90, s90, s91
	s_and_b32 s91, s2, 0xffffff80
	s_or_b32 s90, s90, s91
	s_cmp_lt_u32 s2, 0x180
	s_cselect_b32 s2, s90, s2
	v_lshl_or_b32 v172, s2, 2, v1
	v_and_b32_e32 v211, 31, v0
	v_lshlrev_b32_e32 v178, 5, v172
	v_or_b32_e32 v2, v178, v211
	v_min_i32_e32 v62, 0xc34f, v2
	v_ashrrev_i32_e32 v63, 31, v62
	v_lshlrev_b64 v[4:5], 2, v[62:63]
	v_lshl_add_u64 v[6:7], s[8:9], 0, v[4:5]
	s_waitcnt lgkmcnt(0)
	v_lshl_add_u64 v[4:5], s[12:13], 0, v[4:5]
	global_load_dword v207, v[4:5], off
	v_min_i32_e32 v4, 0x61a, v172
	v_lshlrev_b32_e32 v2, 5, v4
	v_sub_u32_e32 v2, 0xc350, v2
	v_min_u32_e32 v2, 32, v2
	v_add_u32_e32 v22, -1, v2
	v_ashrrev_i32_e32 v5, 31, v4
	v_lshlrev_b32_e32 v2, 2, v0
	v_and_b32_e32 v206, 60, v2
	v_lshlrev_b64 v[4:5], 13, v[4:5]
	v_bfe_u32 v205, v0, 4, 2
	v_lshl_or_b32 v4, v206, 2, v4
	global_load_dwordx2 v[174:175], v[6:7], off
	v_lshl_add_u64 v[6:7], s[16:17], 0, v[4:5]
	v_lshlrev_b32_e32 v2, 8, v205
	v_or_b32_e32 v204, 4, v205
	v_lshl_add_u64 v[8:9], v[6:7], 0, v[2:3]
	v_lshlrev_b32_e32 v10, 8, v204
	v_mov_b32_e32 v11, v3
	v_or_b32_e32 v203, 8, v205
	v_lshl_add_u64 v[12:13], v[6:7], 0, v[10:11]
	global_load_dwordx4 v[132:135], v[8:9], off
	global_load_dwordx4 v[136:139], v[12:13], off
	v_lshlrev_b32_e32 v8, 8, v203
	v_mov_b32_e32 v9, v3
	v_or_b32_e32 v202, 12, v205
	v_lshl_add_u64 v[12:13], v[6:7], 0, v[8:9]
	v_lshlrev_b32_e32 v14, 8, v202
	v_mov_b32_e32 v15, v3
	v_or_b32_e32 v201, 16, v205
	v_lshl_add_u64 v[16:17], v[6:7], 0, v[14:15]
	global_load_dwordx4 v[140:143], v[12:13], off
	global_load_dwordx4 v[144:147], v[16:17], off
	v_min_u32_e32 v12, v201, v22
	v_or_b32_e32 v200, 20, v205
	v_lshlrev_b32_e32 v12, 8, v12
	v_mov_b32_e32 v13, v3
	v_min_u32_e32 v18, v200, v22
	v_lshl_add_u64 v[16:17], v[6:7], 0, v[12:13]
	v_lshlrev_b32_e32 v18, 8, v18
	v_mov_b32_e32 v19, v3
	v_or_b32_e32 v199, 24, v205
	v_or_b32_e32 v198, 28, v205
	v_lshl_add_u64 v[20:21], v[6:7], 0, v[18:19]
	global_load_dwordx4 v[148:151], v[16:17], off
	global_load_dwordx4 v[152:155], v[20:21], off
	v_min_u32_e32 v16, v199, v22
	v_min_u32_e32 v22, v198, v22
	v_lshlrev_b32_e32 v16, 8, v16
	v_mov_b32_e32 v17, v3
	v_lshlrev_b32_e32 v22, 8, v22
	v_mov_b32_e32 v23, v3
	v_lshl_add_u64 v[4:5], s[18:19], 0, v[4:5]
	v_lshl_add_u64 v[20:21], v[6:7], 0, v[16:17]
	v_lshl_add_u64 v[6:7], v[6:7], 0, v[22:23]
	v_lshl_add_u64 v[2:3], v[4:5], 0, v[2:3]
	global_load_dwordx4 v[156:159], v[20:21], off
	global_load_dwordx4 v[160:163], v[6:7], off
	v_lshl_add_u64 v[6:7], v[4:5], 0, v[10:11]
	global_load_dwordx4 v[104:107], v[2:3], off
	global_load_dwordx4 v[100:103], v[6:7], off
	v_lshl_add_u64 v[2:3], v[4:5], 0, v[8:9]
	v_bfe_u32 v177, v0, 5, 1
	v_lshl_add_u64 v[6:7], v[4:5], 0, v[14:15]
	global_load_dwordx4 v[108:111], v[2:3], off
	global_load_dwordx4 v[112:115], v[6:7], off
	v_lshl_add_u64 v[2:3], v[4:5], 0, v[12:13]
	v_lshl_add_u64 v[6:7], v[4:5], 0, v[18:19]
	global_load_dwordx4 v[116:119], v[2:3], off
	global_load_dwordx4 v[120:123], v[6:7], off
	v_lshl_add_u64 v[2:3], v[4:5], 0, v[16:17]
	v_lshl_add_u64 v[4:5], v[4:5], 0, v[22:23]
	v_lshlrev_b32_e32 v212, 4, v177
	global_load_dwordx4 v[128:131], v[2:3], off
	global_load_dwordx4 v[124:127], v[4:5], off
	global_load_dwordx4 v[18:21], v212, s[14:15]
	global_load_dwordx4 v[22:25], v212, s[14:15] offset:32
	global_load_dwordx4 v[26:29], v212, s[14:15] offset:64
	global_load_dwordx4 v[30:33], v212, s[14:15] offset:96
	s_nop 0
	global_load_dwordx4 v[2:5], v212, s[14:15] offset:128
	global_load_dwordx4 v[6:9], v212, s[14:15] offset:160
	global_load_dwordx4 v[10:13], v212, s[14:15] offset:192
	global_load_dwordx4 v[14:17], v212, s[14:15] offset:224
	global_load_dwordx4 v[96:99], v212, s[6:7]
	global_load_dwordx4 v[92:95], v212, s[6:7] offset:32
	global_load_dwordx4 v[88:91], v212, s[6:7] offset:64
	global_load_dwordx4 v[84:87], v212, s[6:7] offset:96
	global_load_dwordx4 v[80:83], v212, s[6:7] offset:128
	global_load_dwordx4 v[42:45], v212, s[6:7] offset:160
	global_load_dwordx4 v[38:41], v212, s[6:7] offset:192
	global_load_dwordx4 v[34:37], v212, s[6:7] offset:224
	s_load_dwordx4 s[12:15], s[0:1], 0x30
	s_waitcnt vmcnt(37)
	ds_write_b128 v176, v[46:49] offset:34816
	s_waitcnt vmcnt(36)
	ds_write_b128 v176, v[50:53] offset:38912
	s_waitcnt vmcnt(35)
	ds_write_b128 v176, v[58:61] offset:43008
	v_cndmask_b32_e64 v46, 0, 1, s[4:5]
	v_ashrrev_i32_e32 v173, 31, v172
	v_cmp_ne_u32_e64 s[6:7], 1, v46
	s_andn2_b64 vcc, exec, s[4:5]
	s_waitcnt vmcnt(34)
	ds_write_b128 v176, v[54:57] offset:47104
	s_cbranch_vccnz .LBB9_5
	s_load_dwordx4 s[16:19], s[0:1], 0x18
	s_waitcnt lgkmcnt(0)
	v_lshl_add_u64 v[46:47], v[62:63], 2, s[16:17]
	global_load_dword v48, v[46:47], off
	v_lshlrev_b32_e32 v46, 2, v177
	v_mov_b32_e32 v47, 0
	v_lshlrev_b32_e32 v46, 2, v46
	s_waitcnt vmcnt(0)
	v_lshlrev_b32_e32 v48, 6, v48
	v_ashrrev_i32_e32 v49, 31, v48
	v_lshl_add_u64 v[48:49], v[48:49], 2, s[18:19]
	v_lshl_add_u64 v[46:47], v[48:49], 0, v[46:47]
	global_load_dwordx4 v[68:71], v[46:47], off
	global_load_dwordx4 v[76:79], v[46:47], off offset:32
	global_load_dwordx4 v[72:75], v[46:47], off offset:64
	global_load_dwordx4 v[64:67], v[46:47], off offset:96
	global_load_dwordx4 v[60:63], v[46:47], off offset:128
	global_load_dwordx4 v[56:59], v[46:47], off offset:160
	global_load_dwordx4 v[52:55], v[46:47], off offset:192
	global_load_dwordx4 v[48:51], v[46:47], off offset:224
	v_add_u32_e32 v46, 0x8800, v176
	ds_write_b128 v46, v[168:171] offset:16384
	ds_write_b128 v46, v[164:167] offset:20480
	s_branch .LBB9_6
